# move 1536 more layer-1 expert weight items from the prologue into the top-k phases (L0: WGs 96-255 waves 0-3, L1: WGs 32-255 waves 0-3)
# speedup vs baseline: 1.0262x; 1.0046x over previous
.LBB0_41:
	v_writelane_b32 v253, s24, 32
	v_writelane_b32 v253, s23, 34
	v_writelane_b32 v253, s22, 36
	s_mov_b32 s3, 0
	v_readlane_b32 s0, v253, 29
	s_lshl_b32 s0, s0, 14
	s_add_i32 s29, s0, 0
	s_cmp_lg_u64 s[48:49], 0
	v_readlane_b32 s4, v253, 30
	s_cselect_b64 s[44:45], -1, 0
	s_abs_i32 s2, s4
	v_cvt_f32_u32_e32 v2, s2
	s_sub_i32 s0, 0, s2
	s_ashr_i32 s6, s4, 31
	v_rcp_iflag_f32_e32 v2, v2
	s_nop 0
	v_mul_f32_e32 v2, 0x4f7ffffe, v2
	v_cvt_u32_f32_e32 v2, v2
	s_nop 0
	v_readfirstlane_b32 s1, v2
	s_mul_i32 s0, s0, s1
	s_mul_hi_u32 s0, s1, s0
	s_add_i32 s7, s1, s0
	s_mul_hi_u32 s0, s7, 0x4200
	s_mul_i32 s0, s0, s2
	s_sub_i32 s0, 0x4200, s0
	s_sub_i32 s1, s0, s2
	s_cmp_ge_u32 s0, s2
	s_cselect_b32 s0, s1, s0
	s_sub_i32 s1, s0, s2
	s_cmp_ge_u32 s0, s2
	s_cselect_b32 s8, s1, s0
	s_add_i32 s0, s4, 0xffffff00
	s_cmp_ge_i32 s0, s8
	s_cselect_b64 s[0:1], -1, 0
	s_cmpk_lt_u32 s8, 0x2101
	s_cselect_b64 s[4:5], -1, 0
	s_sub_i32 s8, 0x4200, s8
	s_and_b64 s[0:1], s[0:1], s[4:5]
	s_and_b64 s[0:1], s[0:1], exec
	s_cselect_b32 s5, s8, 0x4200
	s_add_i32 s0, s5, 0xfffff200
	s_cmp_eq_u32 s2, 0x800
	s_cselect_b32 s5, s0, s5
	v_writelane_b32 v253, s5, 38
	v_writelane_b32 v253, s48, 40
	s_mul_hi_u32 s0, s5, s7
	s_mul_i32 s1, s0, s2
	v_writelane_b32 v253, s49, 41
	v_writelane_b32 v253, s50, 42
	v_writelane_b32 v253, s51, 43
	v_writelane_b32 v253, s52, 44
	v_writelane_b32 v253, s53, 45
	v_writelane_b32 v253, s54, 46
	v_writelane_b32 v253, s55, 47
	s_sub_i32 s1, s5, s1
	v_writelane_b32 v253, s56, 48
	s_add_i32 s4, s0, 1
	s_sub_i32 s5, s1, s2
	v_writelane_b32 v253, s57, 49
	s_cmp_ge_u32 s1, s2
	v_writelane_b32 v253, s58, 50
	s_cselect_b32 s0, s4, s0
	v_writelane_b32 v253, s59, 51
	s_cselect_b32 s1, s5, s1
	s_add_i32 s4, s0, 1
	v_writelane_b32 v253, s60, 52
	s_cmp_ge_u32 s1, s2
	v_writelane_b32 v253, s61, 53
	s_cselect_b32 s0, s4, s0
	v_writelane_b32 v253, s62, 54
	s_xor_b32 s0, s0, s6
	v_writelane_b32 v253, s63, 55
	s_sub_i32 s15, s0, s6
	v_writelane_b32 v253, s29, 56
	s_add_i32 s14, s15, -1
	v_writelane_b32 v253, s44, 57
	s_cmp_lt_i32 s15, 1
	v_readfirstlane_b32 s0, v0
	v_writelane_b32 v253, s45, 58
	s_cbranch_scc1 .LBB0_65
	s_ashr_i32 s0, s0, 6
	s_min_i32 s18, s0, s14
	s_cmpk_gt_i32 s27, 0x7ff
	v_readlane_b32 s0, v253, 26
	s_cselect_b64 s[20:21], -1, 0
	s_add_u32 s0, s0, 0x800000
	v_writelane_b32 v253, s0, 59
	v_mov_b32_e32 v133, 0
	v_readlane_b32 s0, v253, 27
	s_addc_u32 s0, s0, 0
	s_add_i32 s25, 0, 0x21000
	v_writelane_b32 v253, s0, 61
	s_add_i32 s0, 0, 0x21200
	v_writelane_b32 v253, s0, 63
	s_add_i32 s0, 0, 0x21100
	v_writelane_b32 v254, s0, 1
	s_add_i32 s0, 0, 0x21300
	v_writelane_b32 v254, s0, 3
	v_writelane_b32 v254, s27, 5
	v_writelane_b32 v254, s14, 7
	v_writelane_b32 v254, s15, 9
	v_writelane_b32 v254, s18, 11
	v_writelane_b32 v254, s20, 13
	s_mov_b32 s22, 0x42800000
	s_mov_b32 s19, 0
	v_writelane_b32 v254, s21, 14
	s_branch .LBB0_45

.LBB0_876:
	s_and_b64 vcc, exec, s[0:1]
	s_cbranch_vccz .LBB0_893
	s_cmpk_lg_i32 s24, 0x100
	s_cbranch_scc1 .Ltkf_orig
	v_readlane_b32 s0, v254, 20
	v_readfirstlane_b32 s3, v0
	s_lshr_b32 s3, s3, 6
	s_cmp_lg_u32 s0, 0
	s_cbranch_scc0 .Ltkf_l1
	s_cmpk_lt_i32 s27, 0x60
	s_cbranch_scc1 .Ltkf_orig0
	s_cmpk_gt_i32 s3, 3
	s_cbranch_scc1 .LBB0_893
	s_lshl_b32 s0, s27, 2
	s_add_i32 s0, s0, s3
	s_addk_i32 s0, 0x3080
	s_branch .Ltkf_go
.Ltkf_l1:
	s_cmpk_gt_i32 s3, 3
	s_cbranch_scc1 .LBB0_893
	s_lshl_b32 s0, s27, 2
	s_add_i32 s0, s0, s3
	s_addk_i32 s0, 0x3400
	s_branch .Ltkf_go
.Ltkf_orig0:
	s_lshl_b32 s0, s27, 3
	s_add_i32 s0, s0, s3
	s_addk_i32 s0, 0x3f00
	s_branch .Ltkf_go
.Ltkf_orig:
	v_readlane_b32 s0, v254, 20
	v_readlane_b32 s1, v254, 21
	s_andn2_b64 vcc, exec, s[0:1]
	s_cbranch_vccnz .LBB0_893
	s_lshl_b32 s0, s24, 3
	s_abs_i32 s1, s0
	v_cvt_f32_u32_e32 v2, s1
	s_sub_i32 s2, 0, s1
	v_rcp_iflag_f32_e32 v2, v2
	s_nop 0
	v_mul_f32_e32 v2, 0x4f7ffffe, v2
	v_cvt_u32_f32_e32 v2, v2
	s_nop 0
	v_readfirstlane_b32 s3, v2
	s_mul_i32 s2, s2, s3
	s_mul_hi_u32 s2, s3, s2
	s_add_i32 s3, s3, s2
	s_mul_hi_u32 s2, s3, 0x4200
	s_mul_i32 s2, s2, s1
	s_sub_i32 s2, 0x4200, s2
	s_sub_i32 s3, s2, s1
	s_cmp_ge_u32 s2, s1
	s_cselect_b32 s2, s3, s2
	s_sub_i32 s3, s2, s1
	s_cmp_ge_u32 s2, s1
	s_cselect_b32 s4, s3, s2
	s_addk_i32 s0, 0xff00
	s_cmp_ge_i32 s0, s4
	s_cselect_b64 s[0:1], -1, 0
	s_cmpk_lt_u32 s4, 0x2101
	s_cselect_b64 s[2:3], -1, 0
	s_sub_i32 s4, 0x4200, s4
	s_and_b64 s[0:1], s[0:1], s[2:3]
	s_and_b64 s[0:1], s[0:1], exec
	s_cselect_b32 s0, s4, 0x4200
	s_lshl_b32 s1, s27, 3
	v_readlane_b32 s2, v254, 51
	s_add_i32 s1, s2, s1
	s_add_i32 s0, s1, s0
	s_cmpk_gt_i32 s0, 0x41ff
	s_cbranch_scc1 .LBB0_893
.Ltkf_go:
	s_mul_hi_i32 s1, s0, 0x3e0f83e1
	s_lshr_b32 s2, s1, 31
	s_ashr_i32 s6, s1, 11
	s_add_i32 s6, s6, s2
	s_mul_i32 s1, s6, 0x2100
	s_sub_i32 s12, s0, s1
	s_mul_i32 s1, s6, 0x11400000
	s_mul_hi_i32 s0, s6, 0x11400000
	s_add_u32 s1, s62, s1
	s_addc_u32 s0, s26, s0
	s_add_u32 s10, s1, 0x800000
	s_addc_u32 s11, s0, 0
	v_lshlrev_b32_e32 v136, 2, v132
	v_lshrrev_b32_e32 v2, 4, v135
	s_mov_b64 s[0:1], -1
	s_cmpk_gt_i32 s12, 0x15ff
	v_and_b32_e32 v133, 7, v135
	v_and_b32_e32 v137, 0x7c, v136
	v_and_b32_e32 v134, 2, v2
	s_cbranch_scc0 .LBB0_883
	s_add_i32 s0, s12, 0xffffea00
	s_mul_i32 s1, s0, 0xba2f
	s_lshr_b32 s3, s1, 23
	s_mul_i32 s1, s3, 0xffffff50
	s_add_i32 s1, s1, s0
	s_lshl_b32 s0, s1, 4
	s_and_b32 s2, s0, 0xffffff80
	s_lshl_b32 s0, s6, 4
	s_add_i32 s0, s0, s3
	s_mul_hi_i32 s1, s0, 0xb00
	s_mulk_i32 s0, 0xb00
	s_ashr_i32 s4, s2, 31
	s_add_u32 s0, s0, s2
	s_addc_u32 s1, s1, s4
	v_readlane_b32 s16, v253, 40
	s_lshl_b64 s[0:1], s[0:1], 12
	v_readlane_b32 s24, v253, 48
	v_readlane_b32 s25, v253, 49
	s_add_u32 s0, s24, s0
	s_addc_u32 s1, s25, s1
	s_lshl_b32 s5, s12, 7
	s_and_b32 s5, s5, 0x380
	s_lshl_b32 s7, s5, 2
	s_add_u32 s0, s0, s7
	s_addc_u32 s1, s1, 0
	v_lshlrev_b32_e32 v194, 2, v137
	v_readlane_b32 s18, v253, 42
	v_lshl_add_u64 v[2:3], s[0:1], 0, v[194:195]
	v_readlane_b32 s0, v253, 56
	v_lshlrev_b32_e32 v4, 12, v135
	v_and_b32_e32 v139, 0x20000, v4
	v_lshl_add_u32 v138, v137, 7, s0
	s_mov_b32 s7, 0
	s_mov_b64 s[0:1], -1
	s_mov_b32 s9, 0x8000
	s_mov_b32 s13, 0x16000
	s_mov_b32 s14, 0x18000
	s_mov_b32 s15, 0x1e000
	s_mov_b32 s16, 0xc000
	s_mov_b32 s18, 0x42800000
	v_readlane_b32 s17, v253, 41
	v_readlane_b32 s19, v253, 43
	v_readlane_b32 s20, v253, 44
	v_readlane_b32 s21, v253, 45
	v_readlane_b32 s22, v253, 46
	v_readlane_b32 s23, v253, 47
	v_readlane_b32 s26, v253, 50
	v_readlane_b32 s27, v253, 51
	v_readlane_b32 s28, v253, 52
	v_readlane_b32 s29, v253, 53
	v_readlane_b32 s30, v253, 54
	v_readlane_b32 s31, v253, 55
